# v27 + non-temporal (nt) stores in the in_proj epilogue (qkvuz streaming output)
# baseline (speedup 1.0000x reference)
; __device__ __forceinline__ unsigned cvt_pk_bf16(float lo, float hi) { const f32x2_t v = {lo, hi}; return __builtin_bit_cast(unsigned, __builtin_convertvector(v, bf16x2_t)); }
;     __device__ __forceinline__ void operator()(const f32x4 (&acc)[2][2][4][2], const Unit& u, int wr, int wc, int fr, int fq) const {
;         const int row0 = u.t * 256 + wr * 64 + fr, col0 = u.nt * 256 + wc * 32 + 8 * fq;
; #pragma unroll
;         for (int ai = 0; ai < 2; ++ai)
; #pragma unroll
;             for (int m = 0; m < 4; ++m) { bf16_t* rowp = O + (size_t)(row0 + ai * 128 + m * 16) * ldc + col0;
; #pragma unroll
;                 for (int bj = 0; bj < 2; ++bj) { const f32x4 v0 = acc[ai][bj][m][0], v1 = acc[ai][bj][m][1];
;                     u32x4 w; w.x = cvt_pk_bf16(v0[0], v0[1]); w.y = cvt_pk_bf16(v0[2], v0[3]); w.z = cvt_pk_bf16(v1[0], v1[1]); w.w = cvt_pk_bf16(v1[2], v1[3]);
;                     *(u32x4*)(rowp + bj * 128) = w; } }
;     }
.LBB0_199:
	v_lshl_or_b32 v2, s54, 8, v189
	v_lshl_add_u32 v12, s16, 8, v187
	v_ashrrev_i32_e32 v3, 31, v2
	v_mov_b64_e32 v[6:7], s[10:11]
	v_mad_i64_i32 v[4:5], s[28:29], v12, s53, v[6:7]
	v_lshlrev_b64 v[8:9], 1, v[2:3]
	v_lshl_add_u64 v[10:11], v[4:5], 0, v[8:9]
	v_cvt_pk_bf16_f32 v2, v158, v159
	v_cvt_pk_bf16_f32 v3, v160, v161
	v_cvt_pk_bf16_f32 v4, v154, v155
	v_cvt_pk_bf16_f32 v5, v156, v157
	s_nop 15
	s_nop 15
	global_store_dwordx4 v[10:11], v[2:5], off nt
	s_andn2_b64 vcc, exec, s[4:5]
	s_mov_b64 s[4:5], -1
	v_cvt_pk_bf16_f32 v2, v142, v143
	v_cvt_pk_bf16_f32 v3, v144, v145
	v_cvt_pk_bf16_f32 v4, v138, v139
	v_cvt_pk_bf16_f32 v5, v140, v141
	global_store_dwordx4 v[10:11], v[2:5], off offset:256 nt
	s_nop 1
	v_or_b32_e32 v2, 16, v12
	v_mad_i64_i32 v[2:3], s[28:29], v2, s53, v[6:7]
	v_lshl_add_u64 v[10:11], v[2:3], 0, v[8:9]
	v_cvt_pk_bf16_f32 v2, v150, v151
	v_cvt_pk_bf16_f32 v3, v152, v153
	v_cvt_pk_bf16_f32 v4, v146, v147
	v_cvt_pk_bf16_f32 v5, v148, v149
	global_store_dwordx4 v[10:11], v[2:5], off nt
	s_nop 1
	v_cvt_pk_bf16_f32 v2, v126, v127
	v_cvt_pk_bf16_f32 v3, v128, v129
	v_cvt_pk_bf16_f32 v4, v122, v123
	v_cvt_pk_bf16_f32 v5, v124, v125
	global_store_dwordx4 v[10:11], v[2:5], off offset:256 nt
	s_nop 1
	v_or_b32_e32 v2, 32, v12
	v_mad_i64_i32 v[2:3], s[28:29], v2, s53, v[6:7]
	v_lshl_add_u64 v[10:11], v[2:3], 0, v[8:9]
	v_cvt_pk_bf16_f32 v2, v134, v135
	v_cvt_pk_bf16_f32 v3, v136, v137
	v_cvt_pk_bf16_f32 v4, v130, v131
	v_cvt_pk_bf16_f32 v5, v132, v133
	global_store_dwordx4 v[10:11], v[2:5], off nt
	s_nop 1
	v_cvt_pk_bf16_f32 v2, v102, v103
	v_cvt_pk_bf16_f32 v3, v104, v105
	v_cvt_pk_bf16_f32 v4, v90, v91
	v_cvt_pk_bf16_f32 v5, v92, v93
	global_store_dwordx4 v[10:11], v[2:5], off offset:256 nt
	s_nop 1
	v_or_b32_e32 v2, 48, v12
	v_mad_i64_i32 v[2:3], s[28:29], v2, s53, v[6:7]
	v_lshl_add_u64 v[10:11], v[2:3], 0, v[8:9]
	v_cvt_pk_bf16_f32 v2, v118, v119
	v_cvt_pk_bf16_f32 v3, v120, v121
	v_cvt_pk_bf16_f32 v4, v106, v107
	v_cvt_pk_bf16_f32 v5, v108, v109
	global_store_dwordx4 v[10:11], v[2:5], off nt
	s_nop 1
	v_cvt_pk_bf16_f32 v2, v74, v75
	v_cvt_pk_bf16_f32 v3, v76, v77
	v_cvt_pk_bf16_f32 v4, v66, v67
	v_cvt_pk_bf16_f32 v5, v68, v69
	global_store_dwordx4 v[10:11], v[2:5], off offset:256 nt
	s_nop 1
	v_add_u32_e32 v2, 0x80, v12
	v_mad_i64_i32 v[2:3], s[28:29], v2, s53, v[6:7]
	v_lshl_add_u64 v[10:11], v[2:3], 0, v[8:9]
	v_cvt_pk_bf16_f32 v2, v62, v63
	v_cvt_pk_bf16_f32 v3, v64, v65
	v_cvt_pk_bf16_f32 v4, v58, v59
	v_cvt_pk_bf16_f32 v5, v60, v61
	global_store_dwordx4 v[10:11], v[2:5], off nt
	s_nop 1
	v_cvt_pk_bf16_f32 v2, v110, v111
	v_cvt_pk_bf16_f32 v3, v112, v113
	v_cvt_pk_bf16_f32 v4, v114, v115
	v_cvt_pk_bf16_f32 v5, v116, v117
	global_store_dwordx4 v[10:11], v[2:5], off offset:256 nt
	s_nop 1
	v_add_u32_e32 v2, 0x90, v12
	v_mad_i64_i32 v[2:3], s[28:29], v2, s53, v[6:7]
	v_lshl_add_u64 v[10:11], v[2:3], 0, v[8:9]
	v_cvt_pk_bf16_f32 v2, v54, v55
	v_cvt_pk_bf16_f32 v3, v56, v57
	v_cvt_pk_bf16_f32 v4, v50, v51
	v_cvt_pk_bf16_f32 v5, v52, v53
	global_store_dwordx4 v[10:11], v[2:5], off nt
	s_nop 1
	v_cvt_pk_bf16_f32 v2, v94, v95
	v_cvt_pk_bf16_f32 v3, v96, v97
	v_cvt_pk_bf16_f32 v4, v98, v99
	v_cvt_pk_bf16_f32 v5, v100, v101
	global_store_dwordx4 v[10:11], v[2:5], off offset:256 nt
	s_nop 1
	v_add_u32_e32 v2, 0xa0, v12
	v_mad_i64_i32 v[2:3], s[28:29], v2, s53, v[6:7]
	v_lshl_add_u64 v[10:11], v[2:3], 0, v[8:9]
	v_cvt_pk_bf16_f32 v2, v46, v47
	v_cvt_pk_bf16_f32 v3, v48, v49
	v_cvt_pk_bf16_f32 v4, v42, v43
	v_cvt_pk_bf16_f32 v5, v44, v45
	global_store_dwordx4 v[10:11], v[2:5], off nt
	s_nop 1
	v_cvt_pk_bf16_f32 v2, v82, v83
	v_cvt_pk_bf16_f32 v3, v84, v85
	v_cvt_pk_bf16_f32 v4, v86, v87
	v_cvt_pk_bf16_f32 v5, v88, v89
	global_store_dwordx4 v[10:11], v[2:5], off offset:256 nt
	s_nop 1
	v_add_u32_e32 v2, 0xb0, v12
	v_mad_i64_i32 v[2:3], s[28:29], v2, s53, v[6:7]
	v_lshl_add_u64 v[6:7], v[2:3], 0, v[8:9]
	v_cvt_pk_bf16_f32 v2, v38, v39
	v_cvt_pk_bf16_f32 v3, v40, v41
	v_cvt_pk_bf16_f32 v4, v34, v35
	v_cvt_pk_bf16_f32 v5, v36, v37
	global_store_dwordx4 v[6:7], v[2:5], off nt
	s_nop 1
	v_cvt_pk_bf16_f32 v2, v70, v71
	v_cvt_pk_bf16_f32 v3, v72, v73
	v_cvt_pk_bf16_f32 v4, v78, v79
	v_cvt_pk_bf16_f32 v5, v80, v81
	global_store_dwordx4 v[6:7], v[2:5], off offset:256 nt
	s_cbranch_vccnz .LBB0_192
	s_andn2_b64 vcc, exec, s[8:9]
	s_cbranch_vccnz .LBB0_191
	s_barrier
	s_branch .LBB0_191
